# combined: load-early K-loop segments + packed-f32 expert-up epilogue + bias loads hoisted ahead of the epilogue stores (vmcnt(8) before acc init)
# speedup vs baseline: 1.0057x; 1.0057x over previous
.LBB0_1232:
	s_and_b64 vcc, exec, s[8:9]
	s_cbranch_vccnz .Lbh_skip_a
	v_readlane_b32 vcc_lo, v254, 8
	v_readlane_b32 vcc_hi, v254, 9
	s_lshl_b32 s98, s48, 14
	v_mbcnt_lo_u32_b32 v156, -1, 0
	s_add_u32 vcc_lo, vcc_lo, s98
	s_addc_u32 vcc_hi, vcc_hi, 0
	s_lshl_b32 s98, s50, 9
	v_mbcnt_hi_u32_b32 v156, -1, v156
	s_add_u32 vcc_lo, vcc_lo, s98
	s_addc_u32 vcc_hi, vcc_hi, 0
	s_lshl_b32 s98, s5, 2
	v_ashrrev_i32_e32 v156, 1, v156
	s_add_u32 vcc_lo, vcc_lo, s98
	s_addc_u32 vcc_hi, vcc_hi, 0
	v_and_b32_e32 v156, -8, v156
	v_ashrrev_i32_e32 v157, 31, v156
	v_lshl_add_u64 v[156:157], v[156:157], 2, vcc
	s_movk_i32 vcc_lo, 0x2000
	s_mov_b32 vcc_hi, 0
	v_lshl_add_u64 v[158:159], v[156:157], 0, s[18:19]
	global_load_dwordx4 v[148:151], v[156:157], off offset:16
	global_load_dwordx4 v[140:143], v[156:157], off
	v_lshl_add_u64 v[156:157], v[156:157], 0, vcc
	global_load_dwordx4 v[152:155], v[158:159], off offset:16
	global_load_dwordx4 v[144:147], v[156:157], off
.Lbh_skip_a:
	s_add_u32 s58, s2, 0xffffff00
	s_addc_u32 s59, s49, -1
	s_lshl_b32 s2, s43, 2
	s_add_i32 s2, s2, 0
	s_add_i32 s2, s2, 0x24080
	v_mov_b32_e32 v42, v131
	v_mov_b32_e32 v43, s2
	ds_read_b32 v43, v43
	v_mbcnt_lo_u32_b32 v42, -1, v42
	s_lshl_b32 s2, s69, 8
	v_mbcnt_hi_u32_b32 v42, -1, v42
	s_add_i32 s2, s2, s78
	v_ashrrev_i32_e32 v44, 1, v42
	v_and_or_b32 v42, v42, 15, s2
	s_lshl_b32 s34, s26, 7
	s_waitcnt lgkmcnt(0)
	v_add_u32_e32 v136, v42, v43
	v_and_b32_e32 v44, -8, v44
	s_or_b32 s34, s34, s5
	v_add_u32_e32 v134, s34, v44
	v_ashrrev_i32_e32 v137, 31, v136
	v_ashrrev_i32_e32 v135, 31, v134
	s_mov_b64 s[34:35], 0x8000
	s_and_b64 vcc, exec, s[8:9]
	v_lshlrev_b64 v[44:45], 11, v[136:137]
	v_lshl_add_u64 v[44:45], s[16:17], 0, v[44:45]
	v_lshl_add_u64 v[134:135], v[44:45], 0, v[134:135]
	v_mov_b32_e32 v50, 0x43800000
	v_mov_b32_e32 v51, 0x43800000
	v_min_f32_e32 v94, 0x44e00000, v94
	v_min_f32_e32 v95, 0x44e00000, v95
	v_min_f32_e32 v96, 0x44e00000, v96
	v_min_f32_e32 v97, 0x44e00000, v97
	v_pk_mul_f32 v[46:47], v[94:95], s[100:101] op_sel_hi:[1,0]
	v_pk_mul_f32 v[48:49], v[96:97], s[100:101] op_sel_hi:[1,0]
	v_exp_f32_e32 v46, v46
	v_exp_f32_e32 v47, v47
	v_exp_f32_e32 v48, v48
	v_exp_f32_e32 v49, v49
	v_med3_f32 v62, v62, s82, v139
	v_med3_f32 v63, v63, s82, v139
	v_med3_f32 v64, v64, s82, v139
	v_med3_f32 v65, v65, s82, v139
	v_pk_add_f32 v[62:63], v[62:63], v[50:51]
	v_pk_add_f32 v[64:65], v[64:65], v[50:51]
	v_pk_add_f32 v[46:47], v[46:47], 1.0 op_sel_hi:[1,0]
	v_pk_add_f32 v[48:49], v[48:49], 1.0 op_sel_hi:[1,0]
	v_rcp_f32_e32 v46, v46
	v_rcp_f32_e32 v47, v47
	v_rcp_f32_e32 v48, v48
	v_rcp_f32_e32 v49, v49
	v_pk_mul_f32 v[94:95], v[94:95], s[100:101] op_sel:[0,1]
	v_pk_mul_f32 v[96:97], v[96:97], s[100:101] op_sel:[0,1]
	v_pk_mul_f32 v[94:95], v[94:95], v[46:47]
	v_pk_mul_f32 v[96:97], v[96:97], v[48:49]
	v_pk_mul_f32 v[94:95], v[94:95], v[62:63]
	v_pk_mul_f32 v[96:97], v[96:97], v[64:65]
	v_min_f32_e32 v90, 0x44e00000, v90
	v_min_f32_e32 v91, 0x44e00000, v91
	v_min_f32_e32 v92, 0x44e00000, v92
	v_min_f32_e32 v93, 0x44e00000, v93
	v_pk_mul_f32 v[46:47], v[90:91], s[100:101] op_sel_hi:[1,0]
	v_pk_mul_f32 v[48:49], v[92:93], s[100:101] op_sel_hi:[1,0]
	v_exp_f32_e32 v46, v46
	v_exp_f32_e32 v47, v47
	v_exp_f32_e32 v48, v48
	v_exp_f32_e32 v49, v49
	v_med3_f32 v58, v58, s82, v139
	v_med3_f32 v59, v59, s82, v139
	v_med3_f32 v60, v60, s82, v139
	v_med3_f32 v61, v61, s82, v139
	v_pk_add_f32 v[58:59], v[58:59], v[50:51]
	v_pk_add_f32 v[60:61], v[60:61], v[50:51]
	v_pk_add_f32 v[46:47], v[46:47], 1.0 op_sel_hi:[1,0]
	v_pk_add_f32 v[48:49], v[48:49], 1.0 op_sel_hi:[1,0]
	v_rcp_f32_e32 v46, v46
	v_rcp_f32_e32 v47, v47
	v_rcp_f32_e32 v48, v48
	v_rcp_f32_e32 v49, v49
	v_pk_mul_f32 v[90:91], v[90:91], s[100:101] op_sel:[0,1]
	v_pk_mul_f32 v[92:93], v[92:93], s[100:101] op_sel:[0,1]
	v_pk_mul_f32 v[90:91], v[90:91], v[46:47]
	v_pk_mul_f32 v[92:93], v[92:93], v[48:49]
	v_pk_mul_f32 v[90:91], v[90:91], v[58:59]
	v_pk_mul_f32 v[92:93], v[92:93], v[60:61]
	v_mov_b32_e32 v42, v131
	v_mov_b32_e32 v43, v131
	v_cvt_pk_fp8_f32 v42, v94, v95
	v_cvt_pk_fp8_f32 v43, v90, v91
	v_cvt_pk_fp8_f32 v42, v96, v97 op_sel:[0,0,1]
	v_cvt_pk_fp8_f32 v43, v92, v93 op_sel:[0,0,1]
	s_nop 0
	global_store_dwordx2 v[134:135], v[42:43], off sc1
	s_nop 1
	v_lshl_add_u64 v[44:45], v[134:135], 0, s[34:35]
	s_mov_b64 s[34:35], 0x10000
	v_min_f32_e32 v86, 0x44e00000, v86
	v_min_f32_e32 v87, 0x44e00000, v87
	v_min_f32_e32 v88, 0x44e00000, v88
	v_min_f32_e32 v89, 0x44e00000, v89
	v_pk_mul_f32 v[46:47], v[86:87], s[100:101] op_sel_hi:[1,0]
	v_pk_mul_f32 v[48:49], v[88:89], s[100:101] op_sel_hi:[1,0]
	v_exp_f32_e32 v46, v46
	v_exp_f32_e32 v47, v47
	v_exp_f32_e32 v48, v48
	v_exp_f32_e32 v49, v49
	v_med3_f32 v54, v54, s82, v139
	v_med3_f32 v55, v55, s82, v139
	v_med3_f32 v56, v56, s82, v139
	v_med3_f32 v57, v57, s82, v139
	v_pk_add_f32 v[54:55], v[54:55], v[50:51]
	v_pk_add_f32 v[56:57], v[56:57], v[50:51]
	v_pk_add_f32 v[46:47], v[46:47], 1.0 op_sel_hi:[1,0]
	v_pk_add_f32 v[48:49], v[48:49], 1.0 op_sel_hi:[1,0]
	v_rcp_f32_e32 v46, v46
	v_rcp_f32_e32 v47, v47
	v_rcp_f32_e32 v48, v48
	v_rcp_f32_e32 v49, v49
	v_pk_mul_f32 v[86:87], v[86:87], s[100:101] op_sel:[0,1]
	v_pk_mul_f32 v[88:89], v[88:89], s[100:101] op_sel:[0,1]
	v_pk_mul_f32 v[86:87], v[86:87], v[46:47]
	v_pk_mul_f32 v[88:89], v[88:89], v[48:49]
	v_pk_mul_f32 v[86:87], v[86:87], v[54:55]
	v_pk_mul_f32 v[88:89], v[88:89], v[56:57]
	v_min_f32_e32 v82, 0x44e00000, v82
	v_min_f32_e32 v83, 0x44e00000, v83
	v_min_f32_e32 v84, 0x44e00000, v84
	v_min_f32_e32 v85, 0x44e00000, v85
	v_pk_mul_f32 v[46:47], v[82:83], s[100:101] op_sel_hi:[1,0]
	v_pk_mul_f32 v[48:49], v[84:85], s[100:101] op_sel_hi:[1,0]
	v_exp_f32_e32 v46, v46
	v_exp_f32_e32 v47, v47
	v_exp_f32_e32 v48, v48
	v_exp_f32_e32 v49, v49
	v_med3_f32 v176, v176, s82, v139
	v_med3_f32 v177, v177, s82, v139
	v_med3_f32 v178, v178, s82, v139
	v_med3_f32 v179, v179, s82, v139
	v_pk_add_f32 v[176:177], v[176:177], v[50:51]
	v_pk_add_f32 v[178:179], v[178:179], v[50:51]
	v_pk_add_f32 v[46:47], v[46:47], 1.0 op_sel_hi:[1,0]
	v_pk_add_f32 v[48:49], v[48:49], 1.0 op_sel_hi:[1,0]
	v_rcp_f32_e32 v46, v46
	v_rcp_f32_e32 v47, v47
	v_rcp_f32_e32 v48, v48
	v_rcp_f32_e32 v49, v49
	v_pk_mul_f32 v[82:83], v[82:83], s[100:101] op_sel:[0,1]
	v_pk_mul_f32 v[84:85], v[84:85], s[100:101] op_sel:[0,1]
	v_pk_mul_f32 v[82:83], v[82:83], v[46:47]
	v_pk_mul_f32 v[84:85], v[84:85], v[48:49]
	v_pk_mul_f32 v[82:83], v[82:83], v[176:177]
	v_pk_mul_f32 v[84:85], v[84:85], v[178:179]
	v_mov_b32_e32 v42, v131
	v_mov_b32_e32 v43, v131
	v_cvt_pk_fp8_f32 v42, v86, v87
	v_cvt_pk_fp8_f32 v43, v82, v83
	v_cvt_pk_fp8_f32 v42, v88, v89 op_sel:[0,0,1]
	v_cvt_pk_fp8_f32 v43, v84, v85 op_sel:[0,0,1]
	s_nop 0
	global_store_dwordx2 v[44:45], v[42:43], off sc1
	s_nop 1
	v_lshl_add_u64 v[44:45], v[134:135], 0, s[34:35]
	s_mov_b64 s[34:35], 0x18000
	v_min_f32_e32 v78, 0x44e00000, v78
	v_min_f32_e32 v79, 0x44e00000, v79
	v_min_f32_e32 v80, 0x44e00000, v80
	v_min_f32_e32 v81, 0x44e00000, v81
	v_pk_mul_f32 v[46:47], v[78:79], s[100:101] op_sel_hi:[1,0]
	v_pk_mul_f32 v[48:49], v[80:81], s[100:101] op_sel_hi:[1,0]
	v_exp_f32_e32 v46, v46
	v_exp_f32_e32 v47, v47
	v_exp_f32_e32 v48, v48
	v_exp_f32_e32 v49, v49
	v_med3_f32 v172, v172, s82, v139
	v_med3_f32 v173, v173, s82, v139
	v_med3_f32 v174, v174, s82, v139
	v_med3_f32 v175, v175, s82, v139
	v_pk_add_f32 v[172:173], v[172:173], v[50:51]
	v_pk_add_f32 v[174:175], v[174:175], v[50:51]
	v_pk_add_f32 v[46:47], v[46:47], 1.0 op_sel_hi:[1,0]
	v_pk_add_f32 v[48:49], v[48:49], 1.0 op_sel_hi:[1,0]
	v_rcp_f32_e32 v46, v46
	v_rcp_f32_e32 v47, v47
	v_rcp_f32_e32 v48, v48
	v_rcp_f32_e32 v49, v49
	v_pk_mul_f32 v[78:79], v[78:79], s[100:101] op_sel:[0,1]
	v_pk_mul_f32 v[80:81], v[80:81], s[100:101] op_sel:[0,1]
	v_pk_mul_f32 v[78:79], v[78:79], v[46:47]
	v_pk_mul_f32 v[80:81], v[80:81], v[48:49]
	v_pk_mul_f32 v[78:79], v[78:79], v[172:173]
	v_pk_mul_f32 v[80:81], v[80:81], v[174:175]
	v_min_f32_e32 v74, 0x44e00000, v74
	v_min_f32_e32 v75, 0x44e00000, v75
	v_min_f32_e32 v76, 0x44e00000, v76
	v_min_f32_e32 v77, 0x44e00000, v77
	v_pk_mul_f32 v[46:47], v[74:75], s[100:101] op_sel_hi:[1,0]
	v_pk_mul_f32 v[48:49], v[76:77], s[100:101] op_sel_hi:[1,0]
	v_exp_f32_e32 v46, v46
	v_exp_f32_e32 v47, v47
	v_exp_f32_e32 v48, v48
	v_exp_f32_e32 v49, v49
	v_med3_f32 v18, v18, s82, v139
	v_med3_f32 v19, v19, s82, v139
	v_med3_f32 v20, v20, s82, v139
	v_med3_f32 v21, v21, s82, v139
	v_pk_add_f32 v[18:19], v[18:19], v[50:51]
	v_pk_add_f32 v[20:21], v[20:21], v[50:51]
	v_pk_add_f32 v[46:47], v[46:47], 1.0 op_sel_hi:[1,0]
	v_pk_add_f32 v[48:49], v[48:49], 1.0 op_sel_hi:[1,0]
	v_rcp_f32_e32 v46, v46
	v_rcp_f32_e32 v47, v47
	v_rcp_f32_e32 v48, v48
	v_rcp_f32_e32 v49, v49
	v_pk_mul_f32 v[74:75], v[74:75], s[100:101] op_sel:[0,1]
	v_pk_mul_f32 v[76:77], v[76:77], s[100:101] op_sel:[0,1]
	v_pk_mul_f32 v[74:75], v[74:75], v[46:47]
	v_pk_mul_f32 v[76:77], v[76:77], v[48:49]
	v_pk_mul_f32 v[74:75], v[74:75], v[18:19]
	v_pk_mul_f32 v[76:77], v[76:77], v[20:21]
	v_mov_b32_e32 v42, v131
	v_mov_b32_e32 v43, v131
	v_cvt_pk_fp8_f32 v42, v78, v79
	v_cvt_pk_fp8_f32 v43, v74, v75
	v_cvt_pk_fp8_f32 v42, v80, v81 op_sel:[0,0,1]
	v_cvt_pk_fp8_f32 v43, v76, v77 op_sel:[0,0,1]
	s_nop 0
	global_store_dwordx2 v[44:45], v[42:43], off sc1
	s_nop 1
	v_lshl_add_u64 v[44:45], v[134:135], 0, s[34:35]
	s_mov_b64 s[34:35], 0x48000
	v_min_f32_e32 v70, 0x44e00000, v70
	v_min_f32_e32 v71, 0x44e00000, v71
	v_min_f32_e32 v72, 0x44e00000, v72
	v_min_f32_e32 v73, 0x44e00000, v73
	v_pk_mul_f32 v[46:47], v[70:71], s[100:101] op_sel_hi:[1,0]
	v_pk_mul_f32 v[48:49], v[72:73], s[100:101] op_sel_hi:[1,0]
	v_exp_f32_e32 v46, v46
	v_exp_f32_e32 v47, v47
	v_exp_f32_e32 v48, v48
	v_exp_f32_e32 v49, v49
	v_med3_f32 v6, v6, s82, v139
	v_med3_f32 v7, v7, s82, v139
	v_med3_f32 v8, v8, s82, v139
	v_med3_f32 v9, v9, s82, v139
	v_pk_add_f32 v[6:7], v[6:7], v[50:51]
	v_pk_add_f32 v[8:9], v[8:9], v[50:51]
	v_pk_add_f32 v[46:47], v[46:47], 1.0 op_sel_hi:[1,0]
	v_pk_add_f32 v[48:49], v[48:49], 1.0 op_sel_hi:[1,0]
	v_rcp_f32_e32 v46, v46
	v_rcp_f32_e32 v47, v47
	v_rcp_f32_e32 v48, v48
	v_rcp_f32_e32 v49, v49
	v_pk_mul_f32 v[70:71], v[70:71], s[100:101] op_sel:[0,1]
	v_pk_mul_f32 v[72:73], v[72:73], s[100:101] op_sel:[0,1]
	v_pk_mul_f32 v[70:71], v[70:71], v[46:47]
	v_pk_mul_f32 v[72:73], v[72:73], v[48:49]
	v_pk_mul_f32 v[70:71], v[70:71], v[6:7]
	v_pk_mul_f32 v[72:73], v[72:73], v[8:9]
	v_min_f32_e32 v66, 0x44e00000, v66
	v_min_f32_e32 v67, 0x44e00000, v67
	v_min_f32_e32 v68, 0x44e00000, v68
	v_min_f32_e32 v69, 0x44e00000, v69
	v_pk_mul_f32 v[46:47], v[66:67], s[100:101] op_sel_hi:[1,0]
	v_pk_mul_f32 v[48:49], v[68:69], s[100:101] op_sel_hi:[1,0]
	v_exp_f32_e32 v46, v46
	v_exp_f32_e32 v47, v47
	v_exp_f32_e32 v48, v48
	v_exp_f32_e32 v49, v49
	v_med3_f32 v14, v14, s82, v139
	v_med3_f32 v15, v15, s82, v139
	v_med3_f32 v16, v16, s82, v139
	v_med3_f32 v17, v17, s82, v139
	v_pk_add_f32 v[14:15], v[14:15], v[50:51]
	v_pk_add_f32 v[16:17], v[16:17], v[50:51]
	v_pk_add_f32 v[46:47], v[46:47], 1.0 op_sel_hi:[1,0]
	v_pk_add_f32 v[48:49], v[48:49], 1.0 op_sel_hi:[1,0]
	v_rcp_f32_e32 v46, v46
	v_rcp_f32_e32 v47, v47
	v_rcp_f32_e32 v48, v48
	v_rcp_f32_e32 v49, v49
	v_pk_mul_f32 v[66:67], v[66:67], s[100:101] op_sel:[0,1]
	v_pk_mul_f32 v[68:69], v[68:69], s[100:101] op_sel:[0,1]
	v_pk_mul_f32 v[66:67], v[66:67], v[46:47]
	v_pk_mul_f32 v[68:69], v[68:69], v[48:49]
	v_pk_mul_f32 v[66:67], v[66:67], v[14:15]
	v_pk_mul_f32 v[68:69], v[68:69], v[16:17]
	v_mov_b32_e32 v42, v131
	v_mov_b32_e32 v43, v131
	v_cvt_pk_fp8_f32 v42, v70, v71
	v_cvt_pk_fp8_f32 v43, v66, v67
	v_cvt_pk_fp8_f32 v42, v72, v73 op_sel:[0,0,1]
	v_cvt_pk_fp8_f32 v43, v68, v69 op_sel:[0,0,1]
	s_nop 0
	global_store_dwordx2 v[44:45], v[42:43], off sc1
	s_nop 1
	v_lshl_add_u64 v[44:45], v[134:135], 0, s[22:23]
	v_min_f32_e32 v38, 0x44e00000, v38
	v_min_f32_e32 v39, 0x44e00000, v39
	v_min_f32_e32 v40, 0x44e00000, v40
	v_min_f32_e32 v41, 0x44e00000, v41
	v_pk_mul_f32 v[46:47], v[38:39], s[100:101] op_sel_hi:[1,0]
	v_pk_mul_f32 v[48:49], v[40:41], s[100:101] op_sel_hi:[1,0]
	v_exp_f32_e32 v46, v46
	v_exp_f32_e32 v47, v47
	v_exp_f32_e32 v48, v48
	v_exp_f32_e32 v49, v49
	v_med3_f32 v98, v98, s82, v139
	v_med3_f32 v99, v99, s82, v139
	v_med3_f32 v100, v100, s82, v139
	v_med3_f32 v101, v101, s82, v139
	v_pk_add_f32 v[98:99], v[98:99], v[50:51]
	v_pk_add_f32 v[100:101], v[100:101], v[50:51]
	v_pk_add_f32 v[46:47], v[46:47], 1.0 op_sel_hi:[1,0]
	v_pk_add_f32 v[48:49], v[48:49], 1.0 op_sel_hi:[1,0]
	v_rcp_f32_e32 v46, v46
	v_rcp_f32_e32 v47, v47
	v_rcp_f32_e32 v48, v48
	v_rcp_f32_e32 v49, v49
	v_pk_mul_f32 v[38:39], v[38:39], s[100:101] op_sel:[0,1]
	v_pk_mul_f32 v[40:41], v[40:41], s[100:101] op_sel:[0,1]
	v_pk_mul_f32 v[38:39], v[38:39], v[46:47]
	v_pk_mul_f32 v[40:41], v[40:41], v[48:49]
	v_pk_mul_f32 v[38:39], v[38:39], v[98:99]
	v_pk_mul_f32 v[40:41], v[40:41], v[100:101]
	v_min_f32_e32 v34, 0x44e00000, v34
	v_min_f32_e32 v35, 0x44e00000, v35
	v_min_f32_e32 v36, 0x44e00000, v36
	v_min_f32_e32 v37, 0x44e00000, v37
	v_pk_mul_f32 v[46:47], v[34:35], s[100:101] op_sel_hi:[1,0]
	v_pk_mul_f32 v[48:49], v[36:37], s[100:101] op_sel_hi:[1,0]
	v_exp_f32_e32 v46, v46
	v_exp_f32_e32 v47, v47
	v_exp_f32_e32 v48, v48
	v_exp_f32_e32 v49, v49
	v_med3_f32 v102, v102, s82, v139
	v_med3_f32 v103, v103, s82, v139
	v_med3_f32 v104, v104, s82, v139
	v_med3_f32 v105, v105, s82, v139
	v_pk_add_f32 v[102:103], v[102:103], v[50:51]
	v_pk_add_f32 v[104:105], v[104:105], v[50:51]
	v_pk_add_f32 v[46:47], v[46:47], 1.0 op_sel_hi:[1,0]
	v_pk_add_f32 v[48:49], v[48:49], 1.0 op_sel_hi:[1,0]
	v_rcp_f32_e32 v46, v46
	v_rcp_f32_e32 v47, v47
	v_rcp_f32_e32 v48, v48
	v_rcp_f32_e32 v49, v49
	v_pk_mul_f32 v[34:35], v[34:35], s[100:101] op_sel:[0,1]
	v_pk_mul_f32 v[36:37], v[36:37], s[100:101] op_sel:[0,1]
	v_pk_mul_f32 v[34:35], v[34:35], v[46:47]
	v_pk_mul_f32 v[36:37], v[36:37], v[48:49]
	v_pk_mul_f32 v[34:35], v[34:35], v[102:103]
	v_pk_mul_f32 v[36:37], v[36:37], v[104:105]
	v_mov_b32_e32 v42, v131
	v_mov_b32_e32 v43, v131
	v_cvt_pk_fp8_f32 v42, v38, v39
	v_cvt_pk_fp8_f32 v43, v34, v35
	v_cvt_pk_fp8_f32 v42, v40, v41 op_sel:[0,0,1]
	v_cvt_pk_fp8_f32 v43, v36, v37 op_sel:[0,0,1]
	s_nop 0
	global_store_dwordx2 v[44:45], v[42:43], off sc1
	s_nop 1
	v_lshl_add_u64 v[44:45], v[134:135], 0, s[34:35]
	s_mov_b64 s[34:35], 0x50000
	v_min_f32_e32 v30, 0x44e00000, v30
	v_min_f32_e32 v31, 0x44e00000, v31
	v_min_f32_e32 v32, 0x44e00000, v32
	v_min_f32_e32 v33, 0x44e00000, v33
	v_pk_mul_f32 v[46:47], v[30:31], s[100:101] op_sel_hi:[1,0]
	v_pk_mul_f32 v[48:49], v[32:33], s[100:101] op_sel_hi:[1,0]
	v_exp_f32_e32 v46, v46
	v_exp_f32_e32 v47, v47
	v_exp_f32_e32 v48, v48
	v_exp_f32_e32 v49, v49
	v_med3_f32 v106, v106, s82, v139
	v_med3_f32 v107, v107, s82, v139
	v_med3_f32 v108, v108, s82, v139
	v_med3_f32 v109, v109, s82, v139
	v_pk_add_f32 v[106:107], v[106:107], v[50:51]
	v_pk_add_f32 v[108:109], v[108:109], v[50:51]
	v_pk_add_f32 v[46:47], v[46:47], 1.0 op_sel_hi:[1,0]
	v_pk_add_f32 v[48:49], v[48:49], 1.0 op_sel_hi:[1,0]
	v_rcp_f32_e32 v46, v46
	v_rcp_f32_e32 v47, v47
	v_rcp_f32_e32 v48, v48
	v_rcp_f32_e32 v49, v49
	v_pk_mul_f32 v[30:31], v[30:31], s[100:101] op_sel:[0,1]
	v_pk_mul_f32 v[32:33], v[32:33], s[100:101] op_sel:[0,1]
	v_pk_mul_f32 v[30:31], v[30:31], v[46:47]
	v_pk_mul_f32 v[32:33], v[32:33], v[48:49]
	v_pk_mul_f32 v[30:31], v[30:31], v[106:107]
	v_pk_mul_f32 v[32:33], v[32:33], v[108:109]
	v_min_f32_e32 v26, 0x44e00000, v26
	v_min_f32_e32 v27, 0x44e00000, v27
	v_min_f32_e32 v28, 0x44e00000, v28
	v_min_f32_e32 v29, 0x44e00000, v29
	v_pk_mul_f32 v[46:47], v[26:27], s[100:101] op_sel_hi:[1,0]
	v_pk_mul_f32 v[48:49], v[28:29], s[100:101] op_sel_hi:[1,0]
	v_exp_f32_e32 v46, v46
	v_exp_f32_e32 v47, v47
	v_exp_f32_e32 v48, v48
	v_exp_f32_e32 v49, v49
	v_med3_f32 v110, v110, s82, v139
	v_med3_f32 v111, v111, s82, v139
	v_med3_f32 v112, v112, s82, v139
	v_med3_f32 v113, v113, s82, v139
	v_pk_add_f32 v[110:111], v[110:111], v[50:51]
	v_pk_add_f32 v[112:113], v[112:113], v[50:51]
	v_pk_add_f32 v[46:47], v[46:47], 1.0 op_sel_hi:[1,0]
	v_pk_add_f32 v[48:49], v[48:49], 1.0 op_sel_hi:[1,0]
	v_rcp_f32_e32 v46, v46
	v_rcp_f32_e32 v47, v47
	v_rcp_f32_e32 v48, v48
	v_rcp_f32_e32 v49, v49
	v_pk_mul_f32 v[26:27], v[26:27], s[100:101] op_sel:[0,1]
	v_pk_mul_f32 v[28:29], v[28:29], s[100:101] op_sel:[0,1]
	v_pk_mul_f32 v[26:27], v[26:27], v[46:47]
	v_pk_mul_f32 v[28:29], v[28:29], v[48:49]
	v_pk_mul_f32 v[26:27], v[26:27], v[110:111]
	v_pk_mul_f32 v[28:29], v[28:29], v[112:113]
	v_mov_b32_e32 v42, v131
	v_mov_b32_e32 v43, v131
	v_cvt_pk_fp8_f32 v42, v30, v31
	v_cvt_pk_fp8_f32 v43, v26, v27
	v_cvt_pk_fp8_f32 v42, v32, v33 op_sel:[0,0,1]
	v_cvt_pk_fp8_f32 v43, v28, v29 op_sel:[0,0,1]
	s_nop 0
	global_store_dwordx2 v[44:45], v[42:43], off sc1
	s_nop 1
	v_lshl_add_u64 v[44:45], v[134:135], 0, s[34:35]
	s_mov_b64 s[34:35], 0x58000
	v_min_f32_e32 v22, 0x44e00000, v22
	v_min_f32_e32 v23, 0x44e00000, v23
	v_min_f32_e32 v24, 0x44e00000, v24
	v_min_f32_e32 v25, 0x44e00000, v25
	v_pk_mul_f32 v[46:47], v[22:23], s[100:101] op_sel_hi:[1,0]
	v_pk_mul_f32 v[48:49], v[24:25], s[100:101] op_sel_hi:[1,0]
	v_exp_f32_e32 v46, v46
	v_exp_f32_e32 v47, v47
	v_exp_f32_e32 v48, v48
	v_exp_f32_e32 v49, v49
	v_med3_f32 v114, v114, s82, v139
	v_med3_f32 v115, v115, s82, v139
	v_med3_f32 v116, v116, s82, v139
	v_med3_f32 v117, v117, s82, v139
	v_pk_add_f32 v[114:115], v[114:115], v[50:51]
	v_pk_add_f32 v[116:117], v[116:117], v[50:51]
	v_pk_add_f32 v[46:47], v[46:47], 1.0 op_sel_hi:[1,0]
	v_pk_add_f32 v[48:49], v[48:49], 1.0 op_sel_hi:[1,0]
	v_rcp_f32_e32 v46, v46
	v_rcp_f32_e32 v47, v47
	v_rcp_f32_e32 v48, v48
	v_rcp_f32_e32 v49, v49
	v_pk_mul_f32 v[22:23], v[22:23], s[100:101] op_sel:[0,1]
	v_pk_mul_f32 v[24:25], v[24:25], s[100:101] op_sel:[0,1]
	v_pk_mul_f32 v[22:23], v[22:23], v[46:47]
	v_pk_mul_f32 v[24:25], v[24:25], v[48:49]
	v_pk_mul_f32 v[22:23], v[22:23], v[114:115]
	v_pk_mul_f32 v[24:25], v[24:25], v[116:117]
	v_min_f32_e32 v220, 0x44e00000, v220
	v_min_f32_e32 v221, 0x44e00000, v221
	v_min_f32_e32 v222, 0x44e00000, v222
	v_min_f32_e32 v223, 0x44e00000, v223
	v_pk_mul_f32 v[46:47], v[220:221], s[100:101] op_sel_hi:[1,0]
	v_pk_mul_f32 v[48:49], v[222:223], s[100:101] op_sel_hi:[1,0]
	v_exp_f32_e32 v46, v46
	v_exp_f32_e32 v47, v47
	v_exp_f32_e32 v48, v48
	v_exp_f32_e32 v49, v49
	v_med3_f32 v118, v118, s82, v139
	v_med3_f32 v119, v119, s82, v139
	v_med3_f32 v120, v120, s82, v139
	v_med3_f32 v121, v121, s82, v139
	v_pk_add_f32 v[118:119], v[118:119], v[50:51]
	v_pk_add_f32 v[120:121], v[120:121], v[50:51]
	v_pk_add_f32 v[46:47], v[46:47], 1.0 op_sel_hi:[1,0]
	v_pk_add_f32 v[48:49], v[48:49], 1.0 op_sel_hi:[1,0]
	v_rcp_f32_e32 v46, v46
	v_rcp_f32_e32 v47, v47
	v_rcp_f32_e32 v48, v48
	v_rcp_f32_e32 v49, v49
	v_pk_mul_f32 v[220:221], v[220:221], s[100:101] op_sel:[0,1]
	v_pk_mul_f32 v[222:223], v[222:223], s[100:101] op_sel:[0,1]
	v_pk_mul_f32 v[220:221], v[220:221], v[46:47]
	v_pk_mul_f32 v[222:223], v[222:223], v[48:49]
	v_pk_mul_f32 v[220:221], v[220:221], v[118:119]
	v_pk_mul_f32 v[222:223], v[222:223], v[120:121]
	v_mov_b32_e32 v42, v131
	v_mov_b32_e32 v43, v131
	v_cvt_pk_fp8_f32 v42, v22, v23
	v_cvt_pk_fp8_f32 v43, v220, v221
	v_cvt_pk_fp8_f32 v42, v24, v25 op_sel:[0,0,1]
	v_cvt_pk_fp8_f32 v43, v222, v223 op_sel:[0,0,1]
	s_nop 0
	global_store_dwordx2 v[44:45], v[42:43], off sc1
	s_nop 1
	v_lshl_add_u64 v[44:45], v[134:135], 0, s[34:35]
	v_min_f32_e32 v2, 0x44e00000, v2
	v_min_f32_e32 v3, 0x44e00000, v3
	v_min_f32_e32 v4, 0x44e00000, v4
	v_min_f32_e32 v5, 0x44e00000, v5
	v_pk_mul_f32 v[46:47], v[2:3], s[100:101] op_sel_hi:[1,0]
	v_pk_mul_f32 v[48:49], v[4:5], s[100:101] op_sel_hi:[1,0]
	v_exp_f32_e32 v46, v46
	v_exp_f32_e32 v47, v47
	v_exp_f32_e32 v48, v48
	v_exp_f32_e32 v49, v49
	v_med3_f32 v122, v122, s82, v139
	v_med3_f32 v123, v123, s82, v139
	v_med3_f32 v124, v124, s82, v139
	v_med3_f32 v125, v125, s82, v139
	v_pk_add_f32 v[122:123], v[122:123], v[50:51]
	v_pk_add_f32 v[124:125], v[124:125], v[50:51]
	v_pk_add_f32 v[46:47], v[46:47], 1.0 op_sel_hi:[1,0]
	v_pk_add_f32 v[48:49], v[48:49], 1.0 op_sel_hi:[1,0]
	v_rcp_f32_e32 v46, v46
	v_rcp_f32_e32 v47, v47
	v_rcp_f32_e32 v48, v48
	v_rcp_f32_e32 v49, v49
	v_pk_mul_f32 v[2:3], v[2:3], s[100:101] op_sel:[0,1]
	v_pk_mul_f32 v[4:5], v[4:5], s[100:101] op_sel:[0,1]
	v_pk_mul_f32 v[2:3], v[2:3], v[46:47]
	v_pk_mul_f32 v[4:5], v[4:5], v[48:49]
	v_pk_mul_f32 v[2:3], v[2:3], v[122:123]
	v_pk_mul_f32 v[4:5], v[4:5], v[124:125]
	v_min_f32_e32 v10, 0x44e00000, v10
	v_min_f32_e32 v11, 0x44e00000, v11
	v_min_f32_e32 v12, 0x44e00000, v12
	v_min_f32_e32 v13, 0x44e00000, v13
	v_pk_mul_f32 v[46:47], v[10:11], s[100:101] op_sel_hi:[1,0]
	v_pk_mul_f32 v[48:49], v[12:13], s[100:101] op_sel_hi:[1,0]
	v_exp_f32_e32 v46, v46
	v_exp_f32_e32 v47, v47
	v_exp_f32_e32 v48, v48
	v_exp_f32_e32 v49, v49
	v_med3_f32 v126, v126, s82, v139
	v_med3_f32 v127, v127, s82, v139
	v_med3_f32 v128, v128, s82, v139
	v_med3_f32 v129, v129, s82, v139
	v_pk_add_f32 v[126:127], v[126:127], v[50:51]
	v_pk_add_f32 v[128:129], v[128:129], v[50:51]
	v_pk_add_f32 v[46:47], v[46:47], 1.0 op_sel_hi:[1,0]
	v_pk_add_f32 v[48:49], v[48:49], 1.0 op_sel_hi:[1,0]
	v_rcp_f32_e32 v46, v46
	v_rcp_f32_e32 v47, v47
	v_rcp_f32_e32 v48, v48
	v_rcp_f32_e32 v49, v49
	v_pk_mul_f32 v[10:11], v[10:11], s[100:101] op_sel:[0,1]
	v_pk_mul_f32 v[12:13], v[12:13], s[100:101] op_sel:[0,1]
	v_pk_mul_f32 v[10:11], v[10:11], v[46:47]
	v_pk_mul_f32 v[12:13], v[12:13], v[48:49]
	v_pk_mul_f32 v[10:11], v[10:11], v[126:127]
	v_pk_mul_f32 v[12:13], v[12:13], v[128:129]
	v_mov_b32_e32 v42, v131
	v_mov_b32_e32 v43, v131
	v_cvt_pk_fp8_f32 v42, v2, v3
	v_cvt_pk_fp8_f32 v43, v10, v11
	v_cvt_pk_fp8_f32 v42, v4, v5 op_sel:[0,0,1]
	v_cvt_pk_fp8_f32 v43, v12, v13 op_sel:[0,0,1]
	s_nop 0
	global_store_dwordx2 v[44:45], v[42:43], off sc1
	s_nop 1
	s_cbranch_vccnz .LBB0_1236
	s_ashr_i32 s49, s48, 31
	v_readlane_b32 s88, v254, 4
	s_lshl_b64 s[8:9], s[48:49], 14
	v_readlane_b32 s92, v254, 8
	v_readlane_b32 s93, v254, 9
	s_add_u32 s2, s92, s8
	v_mov_b32_e32 v2, v131
	s_addc_u32 s26, s93, s9
	s_lshl_b32 s8, s50, 7
	s_ashr_i32 s9, s8, 31
	v_mbcnt_lo_u32_b32 v2, -1, v2
	s_lshl_b64 s[8:9], s[8:9], 2
	v_mbcnt_hi_u32_b32 v2, -1, v2
	s_add_u32 s2, s2, s8
	s_addc_u32 s9, s26, s9
	s_lshl_b32 s8, s5, 2
	v_ashrrev_i32_e32 v2, 1, v2
	s_add_u32 s8, s2, s8
	v_and_b32_e32 v2, -8, v2
	s_addc_u32 s9, s9, 0
	v_ashrrev_i32_e32 v3, 31, v2
	v_lshl_add_u64 v[6:7], v[2:3], 2, s[8:9]
	v_lshl_add_u64 v[14:15], v[6:7], 0, s[18:19]
	v_add_co_u32_e32 v6, vcc, 0x2000, v6
	v_readlane_b32 s89, v254, 5
	s_nop 0
	v_addc_co_u32_e32 v7, vcc, 0, v7, vcc
	s_nop 0
	s_andn2_b64 vcc, exec, s[28:29]
	v_readlane_b32 s90, v254, 6
	v_readlane_b32 s91, v254, 7
	v_readlane_b32 s94, v254, 10
	v_readlane_b32 s95, v254, 11
	s_cbranch_vccnz .LBB0_1235
	s_barrier

.LBB0_1265:
	s_and_b64 vcc, exec, s[4:5]
	s_cbranch_vccnz .Lbh_skip_b
	v_readlane_b32 vcc_lo, v254, 8
	v_readlane_b32 vcc_hi, v254, 9
	s_lshl_b32 s98, s44, 14
	v_mbcnt_lo_u32_b32 v156, -1, 0
	s_add_u32 vcc_lo, vcc_lo, s98
	s_addc_u32 vcc_hi, vcc_hi, 0
	s_lshl_b32 s98, s46, 9
	v_mbcnt_hi_u32_b32 v156, -1, v156
	s_add_u32 vcc_lo, vcc_lo, s98
	s_addc_u32 vcc_hi, vcc_hi, 0
	s_lshl_b32 s98, s63, 2
	v_ashrrev_i32_e32 v156, 1, v156
	s_add_u32 vcc_lo, vcc_lo, s98
	s_addc_u32 vcc_hi, vcc_hi, 0
	v_and_b32_e32 v156, -8, v156
	v_ashrrev_i32_e32 v157, 31, v156
	v_lshl_add_u64 v[156:157], v[156:157], 2, vcc
	s_movk_i32 vcc_lo, 0x2000
	s_mov_b32 vcc_hi, 0
	v_lshl_add_u64 v[158:159], v[156:157], 0, s[6:7]
	global_load_dwordx4 v[148:151], v[156:157], off offset:16
	global_load_dwordx4 v[140:143], v[156:157], off
	v_lshl_add_u64 v[156:157], v[156:157], 0, vcc
	global_load_dwordx4 v[152:155], v[158:159], off offset:16
	global_load_dwordx4 v[144:147], v[156:157], off
.Lbh_skip_b:
	s_add_u32 s54, s45, 0xffffff00
	s_addc_u32 s55, s47, -1
	s_lshl_b32 s34, s64, 2
	s_add_i32 s34, s34, 0
	s_add_i32 s34, s34, 0x24080
	v_mov_b32_e32 v42, v131
	v_mov_b32_e32 v43, s34
	ds_read_b32 v43, v43
	v_mbcnt_lo_u32_b32 v42, -1, v42
	s_lshl_b32 s34, s65, 8
	v_mbcnt_hi_u32_b32 v42, -1, v42
	s_add_i32 s34, s34, s77
	v_ashrrev_i32_e32 v44, 1, v42
	v_and_or_b32 v42, v42, 15, s34
	s_lshl_b32 s35, s22, 7
	s_waitcnt lgkmcnt(0)
	v_add_u32_e32 v136, v42, v43
	v_and_b32_e32 v44, -8, v44
	s_or_b32 s35, s35, s63
	v_add_u32_e32 v134, s35, v44
	v_ashrrev_i32_e32 v137, 31, v136
	v_ashrrev_i32_e32 v135, 31, v134
	s_mov_b64 s[34:35], 0x8000
	s_and_b64 vcc, exec, s[4:5]
	v_lshlrev_b64 v[44:45], 11, v[136:137]
	v_lshl_add_u64 v[44:45], s[16:17], 0, v[44:45]
	v_lshl_add_u64 v[134:135], v[44:45], 0, v[134:135]
	v_mov_b32_e32 v50, 0x43800000
	v_mov_b32_e32 v51, 0x43800000
	v_min_f32_e32 v94, 0x44e00000, v94
	v_min_f32_e32 v95, 0x44e00000, v95
	v_min_f32_e32 v96, 0x44e00000, v96
	v_min_f32_e32 v97, 0x44e00000, v97
	v_pk_mul_f32 v[46:47], v[94:95], s[100:101] op_sel_hi:[1,0]
	v_pk_mul_f32 v[48:49], v[96:97], s[100:101] op_sel_hi:[1,0]
	v_exp_f32_e32 v46, v46
	v_exp_f32_e32 v47, v47
	v_exp_f32_e32 v48, v48
	v_exp_f32_e32 v49, v49
	v_med3_f32 v62, v62, s81, v139
	v_med3_f32 v63, v63, s81, v139
	v_med3_f32 v64, v64, s81, v139
	v_med3_f32 v65, v65, s81, v139
	v_pk_add_f32 v[62:63], v[62:63], v[50:51]
	v_pk_add_f32 v[64:65], v[64:65], v[50:51]
	v_pk_add_f32 v[46:47], v[46:47], 1.0 op_sel_hi:[1,0]
	v_pk_add_f32 v[48:49], v[48:49], 1.0 op_sel_hi:[1,0]
	v_rcp_f32_e32 v46, v46
	v_rcp_f32_e32 v47, v47
	v_rcp_f32_e32 v48, v48
	v_rcp_f32_e32 v49, v49
	v_pk_mul_f32 v[94:95], v[94:95], s[100:101] op_sel:[0,1]
	v_pk_mul_f32 v[96:97], v[96:97], s[100:101] op_sel:[0,1]
	v_pk_mul_f32 v[94:95], v[94:95], v[46:47]
	v_pk_mul_f32 v[96:97], v[96:97], v[48:49]
	v_pk_mul_f32 v[94:95], v[94:95], v[62:63]
	v_pk_mul_f32 v[96:97], v[96:97], v[64:65]
	v_min_f32_e32 v90, 0x44e00000, v90
	v_min_f32_e32 v91, 0x44e00000, v91
	v_min_f32_e32 v92, 0x44e00000, v92
	v_min_f32_e32 v93, 0x44e00000, v93
	v_pk_mul_f32 v[46:47], v[90:91], s[100:101] op_sel_hi:[1,0]
	v_pk_mul_f32 v[48:49], v[92:93], s[100:101] op_sel_hi:[1,0]
	v_exp_f32_e32 v46, v46
	v_exp_f32_e32 v47, v47
	v_exp_f32_e32 v48, v48
	v_exp_f32_e32 v49, v49
	v_med3_f32 v58, v58, s81, v139
	v_med3_f32 v59, v59, s81, v139
	v_med3_f32 v60, v60, s81, v139
	v_med3_f32 v61, v61, s81, v139
	v_pk_add_f32 v[58:59], v[58:59], v[50:51]
	v_pk_add_f32 v[60:61], v[60:61], v[50:51]
	v_pk_add_f32 v[46:47], v[46:47], 1.0 op_sel_hi:[1,0]
	v_pk_add_f32 v[48:49], v[48:49], 1.0 op_sel_hi:[1,0]
	v_rcp_f32_e32 v46, v46
	v_rcp_f32_e32 v47, v47
	v_rcp_f32_e32 v48, v48
	v_rcp_f32_e32 v49, v49
	v_pk_mul_f32 v[90:91], v[90:91], s[100:101] op_sel:[0,1]
	v_pk_mul_f32 v[92:93], v[92:93], s[100:101] op_sel:[0,1]
	v_pk_mul_f32 v[90:91], v[90:91], v[46:47]
	v_pk_mul_f32 v[92:93], v[92:93], v[48:49]
	v_pk_mul_f32 v[90:91], v[90:91], v[58:59]
	v_pk_mul_f32 v[92:93], v[92:93], v[60:61]
	v_mov_b32_e32 v42, v131
	v_mov_b32_e32 v43, v131
	v_cvt_pk_fp8_f32 v42, v94, v95
	v_cvt_pk_fp8_f32 v43, v90, v91
	v_cvt_pk_fp8_f32 v42, v96, v97 op_sel:[0,0,1]
	v_cvt_pk_fp8_f32 v43, v92, v93 op_sel:[0,0,1]
	s_nop 0
	global_store_dwordx2 v[134:135], v[42:43], off sc1
	s_nop 1
	v_lshl_add_u64 v[44:45], v[134:135], 0, s[34:35]
	s_mov_b64 s[34:35], 0x10000
	v_min_f32_e32 v86, 0x44e00000, v86
	v_min_f32_e32 v87, 0x44e00000, v87
	v_min_f32_e32 v88, 0x44e00000, v88
	v_min_f32_e32 v89, 0x44e00000, v89
	v_pk_mul_f32 v[46:47], v[86:87], s[100:101] op_sel_hi:[1,0]
	v_pk_mul_f32 v[48:49], v[88:89], s[100:101] op_sel_hi:[1,0]
	v_exp_f32_e32 v46, v46
	v_exp_f32_e32 v47, v47
	v_exp_f32_e32 v48, v48
	v_exp_f32_e32 v49, v49
	v_med3_f32 v54, v54, s81, v139
	v_med3_f32 v55, v55, s81, v139
	v_med3_f32 v56, v56, s81, v139
	v_med3_f32 v57, v57, s81, v139
	v_pk_add_f32 v[54:55], v[54:55], v[50:51]
	v_pk_add_f32 v[56:57], v[56:57], v[50:51]
	v_pk_add_f32 v[46:47], v[46:47], 1.0 op_sel_hi:[1,0]
	v_pk_add_f32 v[48:49], v[48:49], 1.0 op_sel_hi:[1,0]
	v_rcp_f32_e32 v46, v46
	v_rcp_f32_e32 v47, v47
	v_rcp_f32_e32 v48, v48
	v_rcp_f32_e32 v49, v49
	v_pk_mul_f32 v[86:87], v[86:87], s[100:101] op_sel:[0,1]
	v_pk_mul_f32 v[88:89], v[88:89], s[100:101] op_sel:[0,1]
	v_pk_mul_f32 v[86:87], v[86:87], v[46:47]
	v_pk_mul_f32 v[88:89], v[88:89], v[48:49]
	v_pk_mul_f32 v[86:87], v[86:87], v[54:55]
	v_pk_mul_f32 v[88:89], v[88:89], v[56:57]
	v_min_f32_e32 v82, 0x44e00000, v82
	v_min_f32_e32 v83, 0x44e00000, v83
	v_min_f32_e32 v84, 0x44e00000, v84
	v_min_f32_e32 v85, 0x44e00000, v85
	v_pk_mul_f32 v[46:47], v[82:83], s[100:101] op_sel_hi:[1,0]
	v_pk_mul_f32 v[48:49], v[84:85], s[100:101] op_sel_hi:[1,0]
	v_exp_f32_e32 v46, v46
	v_exp_f32_e32 v47, v47
	v_exp_f32_e32 v48, v48
	v_exp_f32_e32 v49, v49
	v_med3_f32 v176, v176, s81, v139
	v_med3_f32 v177, v177, s81, v139
	v_med3_f32 v178, v178, s81, v139
	v_med3_f32 v179, v179, s81, v139
	v_pk_add_f32 v[176:177], v[176:177], v[50:51]
	v_pk_add_f32 v[178:179], v[178:179], v[50:51]
	v_pk_add_f32 v[46:47], v[46:47], 1.0 op_sel_hi:[1,0]
	v_pk_add_f32 v[48:49], v[48:49], 1.0 op_sel_hi:[1,0]
	v_rcp_f32_e32 v46, v46
	v_rcp_f32_e32 v47, v47
	v_rcp_f32_e32 v48, v48
	v_rcp_f32_e32 v49, v49
	v_pk_mul_f32 v[82:83], v[82:83], s[100:101] op_sel:[0,1]
	v_pk_mul_f32 v[84:85], v[84:85], s[100:101] op_sel:[0,1]
	v_pk_mul_f32 v[82:83], v[82:83], v[46:47]
	v_pk_mul_f32 v[84:85], v[84:85], v[48:49]
	v_pk_mul_f32 v[82:83], v[82:83], v[176:177]
	v_pk_mul_f32 v[84:85], v[84:85], v[178:179]
	v_mov_b32_e32 v42, v131
	v_mov_b32_e32 v43, v131
	v_cvt_pk_fp8_f32 v42, v86, v87
	v_cvt_pk_fp8_f32 v43, v82, v83
	v_cvt_pk_fp8_f32 v42, v88, v89 op_sel:[0,0,1]
	v_cvt_pk_fp8_f32 v43, v84, v85 op_sel:[0,0,1]
	s_nop 0
	global_store_dwordx2 v[44:45], v[42:43], off sc1
	s_nop 1
	v_lshl_add_u64 v[44:45], v[134:135], 0, s[34:35]
	s_mov_b64 s[34:35], 0x18000
	v_min_f32_e32 v78, 0x44e00000, v78
	v_min_f32_e32 v79, 0x44e00000, v79
	v_min_f32_e32 v80, 0x44e00000, v80
	v_min_f32_e32 v81, 0x44e00000, v81
	v_pk_mul_f32 v[46:47], v[78:79], s[100:101] op_sel_hi:[1,0]
	v_pk_mul_f32 v[48:49], v[80:81], s[100:101] op_sel_hi:[1,0]
	v_exp_f32_e32 v46, v46
	v_exp_f32_e32 v47, v47
	v_exp_f32_e32 v48, v48
	v_exp_f32_e32 v49, v49
	v_med3_f32 v172, v172, s81, v139
	v_med3_f32 v173, v173, s81, v139
	v_med3_f32 v174, v174, s81, v139
	v_med3_f32 v175, v175, s81, v139
	v_pk_add_f32 v[172:173], v[172:173], v[50:51]
	v_pk_add_f32 v[174:175], v[174:175], v[50:51]
	v_pk_add_f32 v[46:47], v[46:47], 1.0 op_sel_hi:[1,0]
	v_pk_add_f32 v[48:49], v[48:49], 1.0 op_sel_hi:[1,0]
	v_rcp_f32_e32 v46, v46
	v_rcp_f32_e32 v47, v47
	v_rcp_f32_e32 v48, v48
	v_rcp_f32_e32 v49, v49
	v_pk_mul_f32 v[78:79], v[78:79], s[100:101] op_sel:[0,1]
	v_pk_mul_f32 v[80:81], v[80:81], s[100:101] op_sel:[0,1]
	v_pk_mul_f32 v[78:79], v[78:79], v[46:47]
	v_pk_mul_f32 v[80:81], v[80:81], v[48:49]
	v_pk_mul_f32 v[78:79], v[78:79], v[172:173]
	v_pk_mul_f32 v[80:81], v[80:81], v[174:175]
	v_min_f32_e32 v74, 0x44e00000, v74
	v_min_f32_e32 v75, 0x44e00000, v75
	v_min_f32_e32 v76, 0x44e00000, v76
	v_min_f32_e32 v77, 0x44e00000, v77
	v_pk_mul_f32 v[46:47], v[74:75], s[100:101] op_sel_hi:[1,0]
	v_pk_mul_f32 v[48:49], v[76:77], s[100:101] op_sel_hi:[1,0]
	v_exp_f32_e32 v46, v46
	v_exp_f32_e32 v47, v47
	v_exp_f32_e32 v48, v48
	v_exp_f32_e32 v49, v49
	v_med3_f32 v18, v18, s81, v139
	v_med3_f32 v19, v19, s81, v139
	v_med3_f32 v20, v20, s81, v139
	v_med3_f32 v21, v21, s81, v139
	v_pk_add_f32 v[18:19], v[18:19], v[50:51]
	v_pk_add_f32 v[20:21], v[20:21], v[50:51]
	v_pk_add_f32 v[46:47], v[46:47], 1.0 op_sel_hi:[1,0]
	v_pk_add_f32 v[48:49], v[48:49], 1.0 op_sel_hi:[1,0]
	v_rcp_f32_e32 v46, v46
	v_rcp_f32_e32 v47, v47
	v_rcp_f32_e32 v48, v48
	v_rcp_f32_e32 v49, v49
	v_pk_mul_f32 v[74:75], v[74:75], s[100:101] op_sel:[0,1]
	v_pk_mul_f32 v[76:77], v[76:77], s[100:101] op_sel:[0,1]
	v_pk_mul_f32 v[74:75], v[74:75], v[46:47]
	v_pk_mul_f32 v[76:77], v[76:77], v[48:49]
	v_pk_mul_f32 v[74:75], v[74:75], v[18:19]
	v_pk_mul_f32 v[76:77], v[76:77], v[20:21]
	v_mov_b32_e32 v42, v131
	v_mov_b32_e32 v43, v131
	v_cvt_pk_fp8_f32 v42, v78, v79
	v_cvt_pk_fp8_f32 v43, v74, v75
	v_cvt_pk_fp8_f32 v42, v80, v81 op_sel:[0,0,1]
	v_cvt_pk_fp8_f32 v43, v76, v77 op_sel:[0,0,1]
	s_nop 0
	global_store_dwordx2 v[44:45], v[42:43], off sc1
	s_nop 1
	v_lshl_add_u64 v[44:45], v[134:135], 0, s[34:35]
	s_mov_b64 s[34:35], 0x48000
	v_min_f32_e32 v70, 0x44e00000, v70
	v_min_f32_e32 v71, 0x44e00000, v71
	v_min_f32_e32 v72, 0x44e00000, v72
	v_min_f32_e32 v73, 0x44e00000, v73
	v_pk_mul_f32 v[46:47], v[70:71], s[100:101] op_sel_hi:[1,0]
	v_pk_mul_f32 v[48:49], v[72:73], s[100:101] op_sel_hi:[1,0]
	v_exp_f32_e32 v46, v46
	v_exp_f32_e32 v47, v47
	v_exp_f32_e32 v48, v48
	v_exp_f32_e32 v49, v49
	v_med3_f32 v6, v6, s81, v139
	v_med3_f32 v7, v7, s81, v139
	v_med3_f32 v8, v8, s81, v139
	v_med3_f32 v9, v9, s81, v139
	v_pk_add_f32 v[6:7], v[6:7], v[50:51]
	v_pk_add_f32 v[8:9], v[8:9], v[50:51]
	v_pk_add_f32 v[46:47], v[46:47], 1.0 op_sel_hi:[1,0]
	v_pk_add_f32 v[48:49], v[48:49], 1.0 op_sel_hi:[1,0]
	v_rcp_f32_e32 v46, v46
	v_rcp_f32_e32 v47, v47
	v_rcp_f32_e32 v48, v48
	v_rcp_f32_e32 v49, v49
	v_pk_mul_f32 v[70:71], v[70:71], s[100:101] op_sel:[0,1]
	v_pk_mul_f32 v[72:73], v[72:73], s[100:101] op_sel:[0,1]
	v_pk_mul_f32 v[70:71], v[70:71], v[46:47]
	v_pk_mul_f32 v[72:73], v[72:73], v[48:49]
	v_pk_mul_f32 v[70:71], v[70:71], v[6:7]
	v_pk_mul_f32 v[72:73], v[72:73], v[8:9]
	v_min_f32_e32 v66, 0x44e00000, v66
	v_min_f32_e32 v67, 0x44e00000, v67
	v_min_f32_e32 v68, 0x44e00000, v68
	v_min_f32_e32 v69, 0x44e00000, v69
	v_pk_mul_f32 v[46:47], v[66:67], s[100:101] op_sel_hi:[1,0]
	v_pk_mul_f32 v[48:49], v[68:69], s[100:101] op_sel_hi:[1,0]
	v_exp_f32_e32 v46, v46
	v_exp_f32_e32 v47, v47
	v_exp_f32_e32 v48, v48
	v_exp_f32_e32 v49, v49
	v_med3_f32 v14, v14, s81, v139
	v_med3_f32 v15, v15, s81, v139
	v_med3_f32 v16, v16, s81, v139
	v_med3_f32 v17, v17, s81, v139
	v_pk_add_f32 v[14:15], v[14:15], v[50:51]
	v_pk_add_f32 v[16:17], v[16:17], v[50:51]
	v_pk_add_f32 v[46:47], v[46:47], 1.0 op_sel_hi:[1,0]
	v_pk_add_f32 v[48:49], v[48:49], 1.0 op_sel_hi:[1,0]
	v_rcp_f32_e32 v46, v46
	v_rcp_f32_e32 v47, v47
	v_rcp_f32_e32 v48, v48
	v_rcp_f32_e32 v49, v49
	v_pk_mul_f32 v[66:67], v[66:67], s[100:101] op_sel:[0,1]
	v_pk_mul_f32 v[68:69], v[68:69], s[100:101] op_sel:[0,1]
	v_pk_mul_f32 v[66:67], v[66:67], v[46:47]
	v_pk_mul_f32 v[68:69], v[68:69], v[48:49]
	v_pk_mul_f32 v[66:67], v[66:67], v[14:15]
	v_pk_mul_f32 v[68:69], v[68:69], v[16:17]
	v_mov_b32_e32 v42, v131
	v_mov_b32_e32 v43, v131
	v_cvt_pk_fp8_f32 v42, v70, v71
	v_cvt_pk_fp8_f32 v43, v66, v67
	v_cvt_pk_fp8_f32 v42, v72, v73 op_sel:[0,0,1]
	v_cvt_pk_fp8_f32 v43, v68, v69 op_sel:[0,0,1]
	s_nop 0
	global_store_dwordx2 v[44:45], v[42:43], off sc1
	s_nop 1
	v_lshl_add_u64 v[44:45], v[134:135], 0, s[18:19]
	v_min_f32_e32 v38, 0x44e00000, v38
	v_min_f32_e32 v39, 0x44e00000, v39
	v_min_f32_e32 v40, 0x44e00000, v40
	v_min_f32_e32 v41, 0x44e00000, v41
	v_pk_mul_f32 v[46:47], v[38:39], s[100:101] op_sel_hi:[1,0]
	v_pk_mul_f32 v[48:49], v[40:41], s[100:101] op_sel_hi:[1,0]
	v_exp_f32_e32 v46, v46
	v_exp_f32_e32 v47, v47
	v_exp_f32_e32 v48, v48
	v_exp_f32_e32 v49, v49
	v_med3_f32 v98, v98, s81, v139
	v_med3_f32 v99, v99, s81, v139
	v_med3_f32 v100, v100, s81, v139
	v_med3_f32 v101, v101, s81, v139
	v_pk_add_f32 v[98:99], v[98:99], v[50:51]
	v_pk_add_f32 v[100:101], v[100:101], v[50:51]
	v_pk_add_f32 v[46:47], v[46:47], 1.0 op_sel_hi:[1,0]
	v_pk_add_f32 v[48:49], v[48:49], 1.0 op_sel_hi:[1,0]
	v_rcp_f32_e32 v46, v46
	v_rcp_f32_e32 v47, v47
	v_rcp_f32_e32 v48, v48
	v_rcp_f32_e32 v49, v49
	v_pk_mul_f32 v[38:39], v[38:39], s[100:101] op_sel:[0,1]
	v_pk_mul_f32 v[40:41], v[40:41], s[100:101] op_sel:[0,1]
	v_pk_mul_f32 v[38:39], v[38:39], v[46:47]
	v_pk_mul_f32 v[40:41], v[40:41], v[48:49]
	v_pk_mul_f32 v[38:39], v[38:39], v[98:99]
	v_pk_mul_f32 v[40:41], v[40:41], v[100:101]
	v_min_f32_e32 v34, 0x44e00000, v34
	v_min_f32_e32 v35, 0x44e00000, v35
	v_min_f32_e32 v36, 0x44e00000, v36
	v_min_f32_e32 v37, 0x44e00000, v37
	v_pk_mul_f32 v[46:47], v[34:35], s[100:101] op_sel_hi:[1,0]
	v_pk_mul_f32 v[48:49], v[36:37], s[100:101] op_sel_hi:[1,0]
	v_exp_f32_e32 v46, v46
	v_exp_f32_e32 v47, v47
	v_exp_f32_e32 v48, v48
	v_exp_f32_e32 v49, v49
	v_med3_f32 v102, v102, s81, v139
	v_med3_f32 v103, v103, s81, v139
	v_med3_f32 v104, v104, s81, v139
	v_med3_f32 v105, v105, s81, v139
	v_pk_add_f32 v[102:103], v[102:103], v[50:51]
	v_pk_add_f32 v[104:105], v[104:105], v[50:51]
	v_pk_add_f32 v[46:47], v[46:47], 1.0 op_sel_hi:[1,0]
	v_pk_add_f32 v[48:49], v[48:49], 1.0 op_sel_hi:[1,0]
	v_rcp_f32_e32 v46, v46
	v_rcp_f32_e32 v47, v47
	v_rcp_f32_e32 v48, v48
	v_rcp_f32_e32 v49, v49
	v_pk_mul_f32 v[34:35], v[34:35], s[100:101] op_sel:[0,1]
	v_pk_mul_f32 v[36:37], v[36:37], s[100:101] op_sel:[0,1]
	v_pk_mul_f32 v[34:35], v[34:35], v[46:47]
	v_pk_mul_f32 v[36:37], v[36:37], v[48:49]
	v_pk_mul_f32 v[34:35], v[34:35], v[102:103]
	v_pk_mul_f32 v[36:37], v[36:37], v[104:105]
	v_mov_b32_e32 v42, v131
	v_mov_b32_e32 v43, v131
	v_cvt_pk_fp8_f32 v42, v38, v39
	v_cvt_pk_fp8_f32 v43, v34, v35
	v_cvt_pk_fp8_f32 v42, v40, v41 op_sel:[0,0,1]
	v_cvt_pk_fp8_f32 v43, v36, v37 op_sel:[0,0,1]
	s_nop 0
	global_store_dwordx2 v[44:45], v[42:43], off sc1
	s_nop 1
	v_lshl_add_u64 v[44:45], v[134:135], 0, s[34:35]
	s_mov_b64 s[34:35], 0x50000
	v_min_f32_e32 v30, 0x44e00000, v30
	v_min_f32_e32 v31, 0x44e00000, v31
	v_min_f32_e32 v32, 0x44e00000, v32
	v_min_f32_e32 v33, 0x44e00000, v33
	v_pk_mul_f32 v[46:47], v[30:31], s[100:101] op_sel_hi:[1,0]
	v_pk_mul_f32 v[48:49], v[32:33], s[100:101] op_sel_hi:[1,0]
	v_exp_f32_e32 v46, v46
	v_exp_f32_e32 v47, v47
	v_exp_f32_e32 v48, v48
	v_exp_f32_e32 v49, v49
	v_med3_f32 v106, v106, s81, v139
	v_med3_f32 v107, v107, s81, v139
	v_med3_f32 v108, v108, s81, v139
	v_med3_f32 v109, v109, s81, v139
	v_pk_add_f32 v[106:107], v[106:107], v[50:51]
	v_pk_add_f32 v[108:109], v[108:109], v[50:51]
	v_pk_add_f32 v[46:47], v[46:47], 1.0 op_sel_hi:[1,0]
	v_pk_add_f32 v[48:49], v[48:49], 1.0 op_sel_hi:[1,0]
	v_rcp_f32_e32 v46, v46
	v_rcp_f32_e32 v47, v47
	v_rcp_f32_e32 v48, v48
	v_rcp_f32_e32 v49, v49
	v_pk_mul_f32 v[30:31], v[30:31], s[100:101] op_sel:[0,1]
	v_pk_mul_f32 v[32:33], v[32:33], s[100:101] op_sel:[0,1]
	v_pk_mul_f32 v[30:31], v[30:31], v[46:47]
	v_pk_mul_f32 v[32:33], v[32:33], v[48:49]
	v_pk_mul_f32 v[30:31], v[30:31], v[106:107]
	v_pk_mul_f32 v[32:33], v[32:33], v[108:109]
	v_min_f32_e32 v26, 0x44e00000, v26
	v_min_f32_e32 v27, 0x44e00000, v27
	v_min_f32_e32 v28, 0x44e00000, v28
	v_min_f32_e32 v29, 0x44e00000, v29
	v_pk_mul_f32 v[46:47], v[26:27], s[100:101] op_sel_hi:[1,0]
	v_pk_mul_f32 v[48:49], v[28:29], s[100:101] op_sel_hi:[1,0]
	v_exp_f32_e32 v46, v46
	v_exp_f32_e32 v47, v47
	v_exp_f32_e32 v48, v48
	v_exp_f32_e32 v49, v49
	v_med3_f32 v110, v110, s81, v139
	v_med3_f32 v111, v111, s81, v139
	v_med3_f32 v112, v112, s81, v139
	v_med3_f32 v113, v113, s81, v139
	v_pk_add_f32 v[110:111], v[110:111], v[50:51]
	v_pk_add_f32 v[112:113], v[112:113], v[50:51]
	v_pk_add_f32 v[46:47], v[46:47], 1.0 op_sel_hi:[1,0]
	v_pk_add_f32 v[48:49], v[48:49], 1.0 op_sel_hi:[1,0]
	v_rcp_f32_e32 v46, v46
	v_rcp_f32_e32 v47, v47
	v_rcp_f32_e32 v48, v48
	v_rcp_f32_e32 v49, v49
	v_pk_mul_f32 v[26:27], v[26:27], s[100:101] op_sel:[0,1]
	v_pk_mul_f32 v[28:29], v[28:29], s[100:101] op_sel:[0,1]
	v_pk_mul_f32 v[26:27], v[26:27], v[46:47]
	v_pk_mul_f32 v[28:29], v[28:29], v[48:49]
	v_pk_mul_f32 v[26:27], v[26:27], v[110:111]
	v_pk_mul_f32 v[28:29], v[28:29], v[112:113]
	v_mov_b32_e32 v42, v131
	v_mov_b32_e32 v43, v131
	v_cvt_pk_fp8_f32 v42, v30, v31
	v_cvt_pk_fp8_f32 v43, v26, v27
	v_cvt_pk_fp8_f32 v42, v32, v33 op_sel:[0,0,1]
	v_cvt_pk_fp8_f32 v43, v28, v29 op_sel:[0,0,1]
	s_nop 0
	global_store_dwordx2 v[44:45], v[42:43], off sc1
	s_nop 1
	v_lshl_add_u64 v[44:45], v[134:135], 0, s[34:35]
	s_mov_b64 s[34:35], 0x58000
	v_min_f32_e32 v22, 0x44e00000, v22
	v_min_f32_e32 v23, 0x44e00000, v23
	v_min_f32_e32 v24, 0x44e00000, v24
	v_min_f32_e32 v25, 0x44e00000, v25
	v_pk_mul_f32 v[46:47], v[22:23], s[100:101] op_sel_hi:[1,0]
	v_pk_mul_f32 v[48:49], v[24:25], s[100:101] op_sel_hi:[1,0]
	v_exp_f32_e32 v46, v46
	v_exp_f32_e32 v47, v47
	v_exp_f32_e32 v48, v48
	v_exp_f32_e32 v49, v49
	v_med3_f32 v114, v114, s81, v139
	v_med3_f32 v115, v115, s81, v139
	v_med3_f32 v116, v116, s81, v139
	v_med3_f32 v117, v117, s81, v139
	v_pk_add_f32 v[114:115], v[114:115], v[50:51]
	v_pk_add_f32 v[116:117], v[116:117], v[50:51]
	v_pk_add_f32 v[46:47], v[46:47], 1.0 op_sel_hi:[1,0]
	v_pk_add_f32 v[48:49], v[48:49], 1.0 op_sel_hi:[1,0]
	v_rcp_f32_e32 v46, v46
	v_rcp_f32_e32 v47, v47
	v_rcp_f32_e32 v48, v48
	v_rcp_f32_e32 v49, v49
	v_pk_mul_f32 v[22:23], v[22:23], s[100:101] op_sel:[0,1]
	v_pk_mul_f32 v[24:25], v[24:25], s[100:101] op_sel:[0,1]
	v_pk_mul_f32 v[22:23], v[22:23], v[46:47]
	v_pk_mul_f32 v[24:25], v[24:25], v[48:49]
	v_pk_mul_f32 v[22:23], v[22:23], v[114:115]
	v_pk_mul_f32 v[24:25], v[24:25], v[116:117]
	v_min_f32_e32 v220, 0x44e00000, v220
	v_min_f32_e32 v221, 0x44e00000, v221
	v_min_f32_e32 v222, 0x44e00000, v222
	v_min_f32_e32 v223, 0x44e00000, v223
	v_pk_mul_f32 v[46:47], v[220:221], s[100:101] op_sel_hi:[1,0]
	v_pk_mul_f32 v[48:49], v[222:223], s[100:101] op_sel_hi:[1,0]
	v_exp_f32_e32 v46, v46
	v_exp_f32_e32 v47, v47
	v_exp_f32_e32 v48, v48
	v_exp_f32_e32 v49, v49
	v_med3_f32 v118, v118, s81, v139
	v_med3_f32 v119, v119, s81, v139
	v_med3_f32 v120, v120, s81, v139
	v_med3_f32 v121, v121, s81, v139
	v_pk_add_f32 v[118:119], v[118:119], v[50:51]
	v_pk_add_f32 v[120:121], v[120:121], v[50:51]
	v_pk_add_f32 v[46:47], v[46:47], 1.0 op_sel_hi:[1,0]
	v_pk_add_f32 v[48:49], v[48:49], 1.0 op_sel_hi:[1,0]
	v_rcp_f32_e32 v46, v46
	v_rcp_f32_e32 v47, v47
	v_rcp_f32_e32 v48, v48
	v_rcp_f32_e32 v49, v49
	v_pk_mul_f32 v[220:221], v[220:221], s[100:101] op_sel:[0,1]
	v_pk_mul_f32 v[222:223], v[222:223], s[100:101] op_sel:[0,1]
	v_pk_mul_f32 v[220:221], v[220:221], v[46:47]
	v_pk_mul_f32 v[222:223], v[222:223], v[48:49]
	v_pk_mul_f32 v[220:221], v[220:221], v[118:119]
	v_pk_mul_f32 v[222:223], v[222:223], v[120:121]
	v_mov_b32_e32 v42, v131
	v_mov_b32_e32 v43, v131
	v_cvt_pk_fp8_f32 v42, v22, v23
	v_cvt_pk_fp8_f32 v43, v220, v221
	v_cvt_pk_fp8_f32 v42, v24, v25 op_sel:[0,0,1]
	v_cvt_pk_fp8_f32 v43, v222, v223 op_sel:[0,0,1]
	s_nop 0
	global_store_dwordx2 v[44:45], v[42:43], off sc1
	s_nop 1
	v_lshl_add_u64 v[44:45], v[134:135], 0, s[34:35]
	v_min_f32_e32 v2, 0x44e00000, v2
	v_min_f32_e32 v3, 0x44e00000, v3
	v_min_f32_e32 v4, 0x44e00000, v4
	v_min_f32_e32 v5, 0x44e00000, v5
	v_pk_mul_f32 v[46:47], v[2:3], s[100:101] op_sel_hi:[1,0]
	v_pk_mul_f32 v[48:49], v[4:5], s[100:101] op_sel_hi:[1,0]
	v_exp_f32_e32 v46, v46
	v_exp_f32_e32 v47, v47
	v_exp_f32_e32 v48, v48
	v_exp_f32_e32 v49, v49
	v_med3_f32 v122, v122, s81, v139
	v_med3_f32 v123, v123, s81, v139
	v_med3_f32 v124, v124, s81, v139
	v_med3_f32 v125, v125, s81, v139
	v_pk_add_f32 v[122:123], v[122:123], v[50:51]
	v_pk_add_f32 v[124:125], v[124:125], v[50:51]
	v_pk_add_f32 v[46:47], v[46:47], 1.0 op_sel_hi:[1,0]
	v_pk_add_f32 v[48:49], v[48:49], 1.0 op_sel_hi:[1,0]
	v_rcp_f32_e32 v46, v46
	v_rcp_f32_e32 v47, v47
	v_rcp_f32_e32 v48, v48
	v_rcp_f32_e32 v49, v49
	v_pk_mul_f32 v[2:3], v[2:3], s[100:101] op_sel:[0,1]
	v_pk_mul_f32 v[4:5], v[4:5], s[100:101] op_sel:[0,1]
	v_pk_mul_f32 v[2:3], v[2:3], v[46:47]
	v_pk_mul_f32 v[4:5], v[4:5], v[48:49]
	v_pk_mul_f32 v[2:3], v[2:3], v[122:123]
	v_pk_mul_f32 v[4:5], v[4:5], v[124:125]
	v_min_f32_e32 v10, 0x44e00000, v10
	v_min_f32_e32 v11, 0x44e00000, v11
	v_min_f32_e32 v12, 0x44e00000, v12
	v_min_f32_e32 v13, 0x44e00000, v13
	v_pk_mul_f32 v[46:47], v[10:11], s[100:101] op_sel_hi:[1,0]
	v_pk_mul_f32 v[48:49], v[12:13], s[100:101] op_sel_hi:[1,0]
	v_exp_f32_e32 v46, v46
	v_exp_f32_e32 v47, v47
	v_exp_f32_e32 v48, v48
	v_exp_f32_e32 v49, v49
	v_med3_f32 v126, v126, s81, v139
	v_med3_f32 v127, v127, s81, v139
	v_med3_f32 v128, v128, s81, v139
	v_med3_f32 v129, v129, s81, v139
	v_pk_add_f32 v[126:127], v[126:127], v[50:51]
	v_pk_add_f32 v[128:129], v[128:129], v[50:51]
	v_pk_add_f32 v[46:47], v[46:47], 1.0 op_sel_hi:[1,0]
	v_pk_add_f32 v[48:49], v[48:49], 1.0 op_sel_hi:[1,0]
	v_rcp_f32_e32 v46, v46
	v_rcp_f32_e32 v47, v47
	v_rcp_f32_e32 v48, v48
	v_rcp_f32_e32 v49, v49
	v_pk_mul_f32 v[10:11], v[10:11], s[100:101] op_sel:[0,1]
	v_pk_mul_f32 v[12:13], v[12:13], s[100:101] op_sel:[0,1]
	v_pk_mul_f32 v[10:11], v[10:11], v[46:47]
	v_pk_mul_f32 v[12:13], v[12:13], v[48:49]
	v_pk_mul_f32 v[10:11], v[10:11], v[126:127]
	v_pk_mul_f32 v[12:13], v[12:13], v[128:129]
	v_mov_b32_e32 v42, v131
	v_mov_b32_e32 v43, v131
	v_cvt_pk_fp8_f32 v42, v2, v3
	v_cvt_pk_fp8_f32 v43, v10, v11
	v_cvt_pk_fp8_f32 v42, v4, v5 op_sel:[0,0,1]
	v_cvt_pk_fp8_f32 v43, v12, v13 op_sel:[0,0,1]
	s_nop 0
	global_store_dwordx2 v[44:45], v[42:43], off sc1
	s_nop 1
	s_cbranch_vccnz .LBB0_1269
	v_readlane_b32 s88, v254, 4
	s_ashr_i32 s45, s44, 31
	v_readlane_b32 s92, v254, 8
	v_readlane_b32 s93, v254, 9
	s_lshl_b64 s[4:5], s[44:45], 14
	s_mov_b64 s[56:57], s[92:93]
	s_add_u32 s22, s56, s4
	v_mov_b32_e32 v2, v131
	s_addc_u32 s34, s57, s5
	s_lshl_b32 s4, s46, 7
	s_ashr_i32 s5, s4, 31
	v_mbcnt_lo_u32_b32 v2, -1, v2
	s_lshl_b64 s[4:5], s[4:5], 2
	v_mbcnt_hi_u32_b32 v2, -1, v2
	s_add_u32 s4, s22, s4
	s_addc_u32 s5, s34, s5
	s_lshl_b32 s22, s63, 2
	v_ashrrev_i32_e32 v2, 1, v2
	s_add_u32 s4, s4, s22
	v_and_b32_e32 v2, -8, v2
	s_addc_u32 s5, s5, 0
	v_ashrrev_i32_e32 v3, 31, v2
	v_lshl_add_u64 v[6:7], v[2:3], 2, s[4:5]
	v_lshl_add_u64 v[14:15], v[6:7], 0, s[6:7]
	v_add_co_u32_e32 v6, vcc, 0x2000, v6
	v_readlane_b32 s89, v254, 5
	s_nop 0
	v_addc_co_u32_e32 v7, vcc, 0, v7, vcc
	s_nop 0
	s_andn2_b64 vcc, exec, s[24:25]
	v_readlane_b32 s90, v254, 6
	v_readlane_b32 s91, v254, 7
	v_readlane_b32 s94, v254, 10
	v_readlane_b32 s95, v254, 11
	s_cbranch_vccnz .LBB0_1268
	s_barrier
